# baseline (speedup 1.0000x reference)
.LBB2_58:
	v_mov_b32_e32 v187, 0x4138aa3b
	v_lshrrev_b32_e32 v38, 3, v115
	v_lshlrev_b32_e32 v40, 5, v0
	v_lshrrev_b32_e32 v107, 4, v110
	s_lshl_b32 s6, s38, 13
	v_and_or_b32 v38, v175, 2, v38
	v_and_b32_e32 v40, 0x180, v40
	v_lshlrev_b32_e32 v41, 3, v0
	s_add_i32 s6, s6, 0x12000
	v_lshlrev_b32_e32 v39, 9, v107
	v_and_or_b32 v40, v41, 24, v40
	v_lshlrev_b32_e32 v38, 5, v38
	v_lshrrev_b32_e32 v37, 3, v0
	v_or3_b32 v39, v40, v39, s6
	v_xor_b32_e32 v40, 32, v38
	v_lshl_add_u32 v191, v110, 5, s39
	v_and_b32_e32 v0, 7, v0
	v_or_b32_e32 v186, v39, v38
	v_or_b32_e32 v188, v39, v40
	v_xor_b32_e32 v40, 64, v38
	v_xor_b32_e32 v38, 0x60, v38
	v_bitop3_b32 v0, v37, v0, 6 bitop3:0x6c
	v_or_b32_e32 v190, v39, v38
	v_and_b32_e32 v1, 0x380, v122
	v_lshlrev_b32_e32 v38, 4, v0
	v_add_u32_e32 v0, s33, v115
	v_or_b32_e32 v189, v39, v40
	v_lshlrev_b32_e32 v34, 2, v34
	v_mov_b32_e32 v35, 0
	v_and_b32_e32 v122, 6, v115
	v_xor_b32_e32 v122, v122, v107
	v_lshlrev_b32_e32 v122, 4, v122
	v_lshl_add_u32 v122, v115, 7, v122
	v_add_u32_e32 v122, s6, v122
	s_mov_b32 s60, 0xffff0000
	s_mov_b32 s61, 0
	s_mov_b32 s62, 0
	s_mov_b32 s63, 0xffff
	s_mov_b32 s64, 0
	s_mov_b32 s65, 0xffff0000
	v_or_b32_e32 v39, s6, v1
	v_add_u32_e32 v192, 0x15f90, v0
	v_lshlrev_b32_e32 v0, 7, v107
	v_and_b32_e32 v1, 0x78, v41
	v_lshl_add_u64 v[126:127], s[30:31], 0, v[34:35]
	v_and_b32_e32 v200, 1, v114
	v_mul_u32_u24_e32 v200, 0x980, v200
	v_add_co_u32_e32 v126, vcc, v126, v200
	s_nop 1
	v_addc_co_u32_e32 v127, vcc, 0, v127, vcc
	v_or3_b32 v193, v1, v0, s39
	v_add_u32_e32 v0, s33, v110
	v_mov_b32_e32 v34, v116
	v_mov_b32_e32 v37, v35
	v_lshl_or_b32 v194, v110, 16, v0
	v_lshl_add_u64 v[0:1], v[34:35], 0, v[36:37]
	v_mov_b32_e32 v36, v35
	v_mov_b32_e32 v76, v35
	v_mov_b32_e32 v77, v35
	v_lshl_add_u64 v[0:1], s[34:35], 0, v[0:1]
	v_mov_b32_e32 v34, v35
	v_mov_b32_e32 v74, v35
	v_mov_b32_e32 v75, v35
	s_mov_b32 s12, 0x3c003c00
	v_mov_b64_e32 v[80:81], v[76:77]
	v_mov_b64_e32 v[84:85], v[76:77]
	v_mov_b64_e32 v[88:89], v[76:77]
	v_mov_b64_e32 v[92:93], v[76:77]
	v_mov_b64_e32 v[96:97], v[76:77]
	v_mov_b64_e32 v[100:101], v[76:77]
	v_mov_b64_e32 v[104:105], v[76:77]
	v_mov_b64_e32 v[56:57], v[36:37]
	v_mov_b64_e32 v[60:61], v[36:37]
	v_mov_b64_e32 v[64:65], v[36:37]
	v_mov_b64_e32 v[68:69], v[36:37]
	v_mov_b64_e32 v[72:73], v[36:37]
	s_or_b32 s47, s40, 0x80
	v_lshl_add_u64 v[0:1], v[0:1], 0, 64
	s_mov_b32 s49, 0
	s_mov_b64 s[30:31], -1
	s_mov_b32 s13, s12
	s_movk_i32 s48, 0x300
	v_lshl_add_u32 v118, v114, 4, v116
	v_mov_b32_e32 v119, v165
	v_mov_b32_e32 v116, 0xc3500
	v_lshlrev_b32_e32 v128, 2, v114
	v_add_u32_e32 v196, v39, v38
	v_mov_b64_e32 v[78:79], v[74:75]
	v_mov_b64_e32 v[82:83], v[74:75]
	v_mov_b64_e32 v[86:87], v[74:75]
	v_mov_b64_e32 v[90:91], v[74:75]
	v_mov_b64_e32 v[94:95], v[74:75]
	v_mov_b64_e32 v[98:99], v[74:75]
	v_mov_b64_e32 v[102:103], v[74:75]
	v_mov_b64_e32 v[54:55], v[34:35]
	v_mov_b64_e32 v[58:59], v[34:35]
	v_mov_b64_e32 v[62:63], v[34:35]
	v_mov_b64_e32 v[66:67], v[34:35]
	v_mov_b32_e32 v197, 0
	s_mov_b32 s50, 0
	v_mov_b64_e32 v[70:71], v[34:35]
	v_mov_b32_e32 v50, v35
	v_mov_b32_e32 v51, v35
	v_mov_b32_e32 v52, v35
	v_mov_b32_e32 v53, v35
	v_mov_b32_e32 v46, v35
	v_mov_b32_e32 v47, v35
	v_mov_b32_e32 v48, v35
	v_mov_b32_e32 v49, v35
	v_mov_b32_e32 v42, v35
	v_mov_b32_e32 v43, v35
	v_mov_b32_e32 v44, v35
	v_mov_b32_e32 v45, v35
	v_mov_b32_e32 v38, v35
	v_mov_b32_e32 v39, v35
	v_mov_b32_e32 v40, v35
	v_mov_b32_e32 v41, v35
	s_waitcnt vmcnt(0)
	ds_write_b128 v196, v[10:13]
	ds_write_b128 v196, v[14:17] offset:1024
	ds_write_b128 v196, v[30:33] offset:2048
	ds_write_b128 v196, v[26:29] offset:3072
	ds_write_b128 v196, v[2:5] offset:4096
	ds_write_b128 v196, v[6:9] offset:5120
	ds_write_b128 v196, v[18:21] offset:6144
	ds_write_b128 v196, v[22:25] offset:7168
	s_mul_i32 s78, s42, 0xc00
	s_add_i32 s78, s78, s40
	v_mov_b32_e32 v183, v121
	s_lshl_b32 s6, s43, 6
	s_sub_i32 s83, s44, s6
	s_lshl_b32 s6, s43, 8
	s_add_i32 s82, s78, s6
	v_add_u32_e32 v229, s82, v172
	v_add_u32_e32 v230, s82, v173
	ds_read_u16 v224, v229 offset:0
	ds_read_u16 v225, v229 offset:32
	ds_read_u16 v226, v229 offset:64
	ds_read_u16 v227, v229 offset:96
	ds_read_u16 v232, v229 offset:128
	ds_read_u16 v233, v229 offset:160
	ds_read_u16 v234, v229 offset:192
	ds_read_u16 v235, v229 offset:224
	ds_read_b32 v183, v230
	s_waitcnt lgkmcnt(0)
	s_mov_b32 s85, s83

.Lmk_p72:
	v_and_b32_e32 v200, 1, v114
	v_cmp_eq_u32_e32 vcc, 1, v200
	s_nop 1
	v_cndmask_b32_e32 v124, v124, v174, vcc
	s_cmp_lt_u32 s38, 4
	s_cbranch_scc0 .Lmk_prio_done
	s_setprio 1

.LBB2_93:
	s_lshl_b32 s0, s50, 7
	s_add_i32 s0, s0, 0x26000
	v_lshl_add_u32 v36, v107, 4, s0
	ds_read_b128 v[240:243], v36
	ds_read_b128 v[244:247], v36 offset:64
	s_cmp_gt_i32 s50, 35
	v_mov_b32_e32 v125, 0
	s_cbranch_scc1 .LBB2_103
	v_mov_b32_dpp v174, v124 quad_perm:[1,1,1,1] row_mask:0xf bank_mask:0xf
	v_mov_b32_dpp v124, v124 quad_perm:[0,0,0,0] row_mask:0xf bank_mask:0xf
	v_sub_u32_e32 v125, v174, v124
	s_add_i32 s0, s50, 2
	v_mov_b32_e32 v74, 0
	v_cndmask_b32_e64 v34, 0, v125, s[2:3]
	s_mul_i32 s0, s0, 0xc3500
	v_lshl_add_u32 v36, v124, 2, v118
	v_add_u32_dpp v34, v34, v34 row_shr:1 row_mask:0xf bank_mask:0xf bound_ctrl:1
	s_add_u32 s0, s90, s0
	s_addc_u32 s1, s91, 0
	v_add_u32_dpp v34, v34, v34 row_shr:2 row_mask:0xf bank_mask:0xf bound_ctrl:1
	v_mov_b32_e32 v120, v124
	s_nop 0
	v_add_u32_dpp v34, v34, v34 row_shr:4 row_mask:0xf bank_mask:0xf bound_ctrl:1
	global_load_dwordx4 v[164:167], v36, s[0:1]
	s_nop 0
	v_add_u32_dpp v34, v34, v34 row_shr:8 row_mask:0xf bank_mask:0xf bound_ctrl:1
	s_nop 1
	v_add_u32_dpp v34, v34, v34 row_bcast:15 row_mask:0xa bank_mask:0xf
	s_nop 1
	v_mov_b32_dpp v74, v34 row_bcast:31 row_mask:0xc bank_mask:0xf
	v_sub_u32_e32 v36, v74, v125
	v_add_u32_e32 v129, v36, v34
	v_sub_u32_e32 v36, 0x2f0, v129
	v_min_i32_e32 v125, v125, v36
.LBB2_103:
	s_cmp_gt_i32 s50, 34
	s_cbranch_scc1 .LBB2_105
	s_add_i32 s0, s50, 3
	s_add_u32 s10, s26, s0
	s_addc_u32 s11, s27, 0
	s_lshl_b64 s[10:11], s[10:11], 6
	v_lshl_add_u64 v[36:37], v[126:127], 0, s[10:11]
	global_load_dword v124, v[36:37], off
.LBB2_105:
	s_lshl_b32 s0, s50, 13
	v_lshl_add_u32 v36, v110, 4, s0
	v_mov_b32_e32 v197, v184
	global_load_dwordx4 v[86:89], v36, s[16:17]
	global_load_dwordx4 v[82:85], v36, s[16:17] offset:1024
	global_load_dwordx4 v[78:81], v36, s[16:17] offset:2048
	global_load_dwordx4 v[74:77], v36, s[16:17] offset:3072
	v_add_u32_e32 v37, 0x1000, v36
	v_cvt_f32_f16_e32 v184, v199
	global_load_dwordx4 v[90:93], v37, s[16:17]
	global_load_dwordx4 v[94:97], v37, s[16:17] offset:1024
	global_load_dwordx4 v[98:101], v37, s[16:17] offset:2048
	global_load_dwordx4 v[102:105], v37, s[16:17] offset:3072
	s_cmp_gt_u32 s50, 35
	s_cbranch_scc1 .LBB2_64
	s_mul_i32 s0, s50, 0x1d4c0
	s_add_i32 s0, s0, 0x1d4c0
	v_lshl_add_u32 v34, v192, 1, s0
	global_load_ushort v199, v34, s[24:25]
	s_branch .LBB2_64
